# x14: layer-1 output row pass run by the idle workgroups during the WKV scan, gated on per-scan progress flags; phase 14 skipped
# baseline (speedup 1.0000x reference)
.LBB0_1720:
	s_waitcnt vmcnt(0)
	s_barrier
	s_lshl_b32 s101, s83, 2
	s_add_i32 s101, s101, 0xc400
	v_cmp_eq_u32_e32 vcc, 0, v0
	s_and_saveexec_b64 s[98:99], vcc
	s_cbranch_execz .Lx14_fin_skip
	v_mov_b32_e32 v18, s101
	v_mov_b32_e32 v19, 0x104
	global_store_dword v18, v19, s[54:55] sc1
.Lx14_fin_skip:
	s_or_b64 exec, exec, s[98:99]
	s_add_i32 s83, s83, s33
	s_cmpk_lt_i32 s83, 0x80
	s_waitcnt vmcnt(0) lgkmcnt(0)
	s_barrier
	s_cbranch_scc0 .LBB0_1770

.LBB0_1725:
	s_add_i32 s71, s71, 1
	s_cmpk_eq_i32 s71, 0x104
	s_waitcnt vmcnt(16)
	s_barrier
	s_cbranch_scc1 .LBB0_1736
.LBB0_1726:
	s_add_i32 s100, s71, -1
	s_lshl_b32 s101, s83, 2
	s_add_i32 s101, s101, 0xc400
	v_cmp_eq_u32_e32 vcc, 0, v0
	s_and_saveexec_b64 s[98:99], vcc
	s_cbranch_execz .Lx14_pub_skip
	v_mov_b32_e32 v18, s101
	v_mov_b32_e32 v19, s100
	global_store_dword v18, v19, s[54:55] sc1
.Lx14_pub_skip:
	s_or_b64 exec, exec, s[98:99]
	s_and_b32 s0, s71, 1
	s_lshl_b32 s1, s0, 13
	s_add_i32 s1, s62, s1
	v_add_u32_e32 v18, s1, v159
	v_add_u32_e32 v18, 0x400, v18
	v_mov_b32_e32 v22, s1
	ds_read2_b32 v[180:181], v18 offset1:16
	ds_read2_b32 v[178:179], v18 offset0:32 offset1:48
	ds_read2_b32 v[176:177], v18 offset0:64 offset1:80
	ds_read2_b32 v[174:175], v18 offset0:96 offset1:112
	ds_read2_b32 v[172:173], v18 offset0:128 offset1:144
	ds_read2_b32 v[170:171], v18 offset0:160 offset1:176
	ds_read2_b32 v[168:169], v18 offset0:192 offset1:208
	ds_read2_b32 v[166:167], v18 offset0:224 offset1:240
	ds_read_b128 v[152:155], v22 offset:64
	ds_read_b128 v[148:151], v22 offset:128
	ds_read_b128 v[144:147], v22 offset:192
	ds_read_b128 v[140:143], v22 offset:256
	ds_read_b128 v[136:139], v22 offset:320
	ds_read_b128 v[132:135], v22 offset:336
	ds_read_b128 v[124:127], v22 offset:384
	ds_read_b128 v[120:123], v22 offset:400
	ds_read_b128 v[116:119], v22 offset:448
	ds_read_b128 v[112:115], v22 offset:464
	ds_read_b128 v[108:111], v22 offset:512
	ds_read_b128 v[104:107], v22 offset:528
	ds_read_b128 v[100:103], v22 offset:576
	ds_read_b128 v[96:99], v22 offset:592
	ds_read_b128 v[92:95], v22 offset:608
	ds_read_b128 v[88:91], v22 offset:640
	ds_read_b128 v[84:87], v22 offset:656
	ds_read_b128 v[80:83], v22 offset:672
	ds_read_b128 v[72:75], v22 offset:704
	ds_read_b128 v[68:71], v22 offset:720
	ds_read_b128 v[64:67], v22 offset:736
	ds_read_b128 v[60:63], v22 offset:768
	ds_read_b128 v[56:59], v22 offset:784
	ds_read_b128 v[52:55], v22 offset:800
	ds_read_b128 v[48:51], v22 offset:832
	ds_read_b128 v[44:47], v22 offset:848
	ds_read_b128 v[40:43], v22 offset:864
	ds_read_b128 v[36:39], v22 offset:880
	ds_read_b128 v[32:35], v22 offset:896
	ds_read_b128 v[28:31], v22 offset:912
	ds_read_b128 v[24:27], v22 offset:928
	ds_read_b128 v[18:21], v22 offset:944
	s_waitcnt lgkmcnt(14)
	ds_read_b128 v[154:157], v22 offset:960
	ds_read_b128 v[128:131], v22 offset:976
	ds_read_b128 v[76:79], v22 offset:992
	s_waitcnt lgkmcnt(3)
	ds_read_b128 v[20:23], v22 offset:1008
	s_waitcnt lgkmcnt(0)
	s_mul_i32 s0, s0, 0xcc00
	s_add_i32 s74, s0, 0
	s_and_saveexec_b64 s[68:69], s[8:9]
	s_cbranch_execz .LBB0_1728
	s_waitcnt lgkmcnt(0)
	v_cndmask_b32_e64 v23, v167, v250, s[6:7]
	v_cndmask_b32_e64 v37, v180, v251, s[6:7]
	v_cndmask_b32_e64 v38, v181, v252, s[6:7]
	v_cndmask_b32_e64 v39, v178, v253, s[6:7]
	v_cndmask_b32_e64 v67, v179, v254, s[6:7]
	v_cndmask_b32_e64 v82, v176, v189, s[6:7]
	v_cndmask_b32_e64 v83, v177, v195, s[6:7]
	v_cndmask_b32_e64 v93, v174, v196, s[6:7]
	v_cndmask_b32_e64 v94, v175, v197, s[6:7]
	v_cndmask_b32_e64 v95, v172, v200, s[6:7]
	v_fmac_f32_e32 v23, v37, v154
	v_fmac_f32_e32 v38, v37, v152
	v_fmac_f32_e32 v39, v37, v148
	v_fmac_f32_e32 v67, v37, v144
	v_fmac_f32_e32 v82, v37, v140
	v_fmac_f32_e32 v83, v37, v136
	v_fmac_f32_e32 v93, v37, v124
	v_fmac_f32_e32 v94, v37, v116
	v_fmac_f32_e32 v95, v37, v108
	v_fmac_f32_e32 v23, v38, v155
	v_fmac_f32_e32 v39, v149, v38
	v_fmac_f32_e32 v67, v38, v145
	v_fmac_f32_e32 v82, v38, v141
	v_fmac_f32_e32 v83, v38, v137
	v_fmac_f32_e32 v93, v38, v125
	v_fmac_f32_e32 v94, v38, v117
	v_fmac_f32_e32 v95, v38, v109
	v_fmac_f32_e32 v23, v39, v156
	v_fmac_f32_e32 v67, v146, v39
	v_fmac_f32_e32 v82, v142, v39
	v_fmac_f32_e32 v83, v39, v138
	v_fmac_f32_e32 v93, v39, v126
	v_fmac_f32_e32 v94, v39, v118
	v_fmac_f32_e32 v95, v39, v110
	v_fmac_f32_e32 v23, v67, v157
	v_fmac_f32_e32 v82, v143, v67
	v_fmac_f32_e32 v83, v139, v67
	v_fmac_f32_e32 v93, v67, v127
	v_fmac_f32_e32 v94, v67, v119
	v_fmac_f32_e32 v95, v67, v111
	v_fmac_f32_e32 v23, v82, v128
	v_fmac_f32_e32 v83, v132, v82
	v_fmac_f32_e32 v93, v120, v82
	v_fmac_f32_e32 v94, v82, v112
	v_fmac_f32_e32 v95, v82, v104
	v_fmac_f32_e32 v23, v83, v129
	v_fmac_f32_e32 v93, v121, v83
	v_fmac_f32_e32 v94, v113, v83
	v_fmac_f32_e32 v95, v83, v105
	v_fmac_f32_e32 v23, v93, v130
	v_fmac_f32_e32 v94, v114, v93
	v_fmac_f32_e32 v95, v106, v93
	v_fmac_f32_e32 v23, v94, v131
	v_fmac_f32_e32 v95, v107, v94
	v_fmac_f32_e32 v23, v95, v76
	v_cndmask_b32_e64 v76, v173, v201, s[6:7]
	v_fmac_f32_e32 v76, v37, v100
	v_fmac_f32_e32 v76, v38, v101
	v_fmac_f32_e32 v76, v39, v102
	v_fmac_f32_e32 v76, v67, v103
	v_fmac_f32_e32 v76, v82, v96
	v_fmac_f32_e32 v76, v83, v97
	v_fmac_f32_e32 v76, v93, v98
	v_fmac_f32_e32 v76, v99, v94
	v_fmac_f32_e32 v76, v92, v95
	v_fmac_f32_e32 v23, v76, v77
	v_cndmask_b32_e64 v77, v170, v202, s[6:7]
	v_fmac_f32_e32 v77, v37, v88
	v_fmac_f32_e32 v77, v38, v89
	v_fmac_f32_e32 v77, v39, v90
	v_fmac_f32_e32 v77, v67, v91
	v_fmac_f32_e32 v77, v82, v84
	v_fmac_f32_e32 v77, v83, v85
	v_fmac_f32_e32 v77, v93, v86
	v_fmac_f32_e32 v77, v94, v87
	v_fmac_f32_e32 v77, v80, v95
	v_fmac_f32_e32 v77, v81, v76
	v_fmac_f32_e32 v23, v77, v78
	v_cndmask_b32_e64 v78, v171, v204, s[6:7]
	v_fmac_f32_e32 v78, v37, v72
	v_fmac_f32_e32 v78, v38, v73
	v_fmac_f32_e32 v78, v39, v74
	v_fmac_f32_e32 v78, v67, v75
	v_fmac_f32_e32 v78, v82, v68
	v_fmac_f32_e32 v78, v83, v69
	v_fmac_f32_e32 v78, v93, v70
	v_fmac_f32_e32 v78, v94, v71
	v_fmac_f32_e32 v78, v95, v64
	v_cndmask_b32_e64 v64, v168, v205, s[6:7]
	v_fmac_f32_e32 v64, v37, v60
	v_fmac_f32_e32 v64, v38, v61
	v_fmac_f32_e32 v64, v39, v62
	v_fmac_f32_e32 v64, v67, v63
	v_fmac_f32_e32 v64, v82, v56
	v_fmac_f32_e32 v64, v83, v57
	v_fmac_f32_e32 v64, v93, v58
	v_fmac_f32_e32 v64, v94, v59
	v_fmac_f32_e32 v64, v95, v52
	v_fmac_f32_e32 v78, v65, v76
	v_fmac_f32_e32 v64, v76, v53
	v_fmac_f32_e32 v78, v66, v77
	v_fmac_f32_e32 v64, v54, v77
	v_fmac_f32_e32 v23, v78, v79
	v_fmac_f32_e32 v64, v55, v78
	v_fmac_f32_e32 v23, v64, v20
	v_cndmask_b32_e64 v20, v169, v206, s[6:7]
	v_fmac_f32_e32 v20, v37, v48
	v_fmac_f32_e32 v20, v38, v49
	v_fmac_f32_e32 v20, v39, v50
	v_fmac_f32_e32 v20, v67, v51
	v_fmac_f32_e32 v20, v82, v44
	v_fmac_f32_e32 v20, v83, v45
	v_fmac_f32_e32 v20, v93, v46
	v_fmac_f32_e32 v20, v94, v47
	v_fmac_f32_e32 v20, v95, v40
	v_fmac_f32_e32 v20, v76, v41
	v_fmac_f32_e32 v20, v77, v42
	v_fmac_f32_e32 v20, v43, v78
	v_fmac_f32_e32 v20, v36, v64
	v_fmac_f32_e32 v23, v21, v20
	v_cndmask_b32_e64 v21, v166, v209, s[6:7]
	v_fmac_f32_e32 v21, v37, v32
	v_fmac_f32_e32 v21, v38, v33
	v_fmac_f32_e32 v21, v39, v34
	v_fmac_f32_e32 v21, v67, v35
	v_fmac_f32_e32 v21, v82, v28
	v_fmac_f32_e32 v21, v83, v29
	v_fmac_f32_e32 v21, v93, v30
	v_fmac_f32_e32 v21, v94, v31
	v_fmac_f32_e32 v21, v95, v24
	v_fmac_f32_e32 v21, v76, v25
	v_fmac_f32_e32 v21, v77, v26
	s_mul_i32 s0, s82, 0x3300
	v_fmac_f32_e32 v21, v78, v27
	s_add_i32 s0, s74, s0
	v_fmac_f32_e32 v21, v18, v64
	v_add_u32_e32 v18, s0, v163
	v_fmac_f32_e32 v21, v19, v20
	v_add3_u32 v18, v18, v182, v183
	v_cvt_pk_bf16_f32 v19, v37, s0
	ds_write_b16 v18, v19 offset:8704
	v_cvt_pk_bf16_f32 v19, v38, s0
	ds_write_b16 v18, v19 offset:8768
	v_cvt_pk_bf16_f32 v19, v39, s0
	ds_write_b16 v18, v19 offset:8832
	v_cvt_pk_bf16_f32 v19, v67, s0
	ds_write_b16 v18, v19 offset:8896
	v_cvt_pk_bf16_f32 v19, v82, s0
	ds_write_b16 v18, v19 offset:8960
	v_cvt_pk_bf16_f32 v19, v83, s0
	ds_write_b16 v18, v19 offset:9024
	v_cvt_pk_bf16_f32 v19, v93, s0
	ds_write_b16 v18, v19 offset:9088
	v_cvt_pk_bf16_f32 v19, v94, s0
	ds_write_b16 v18, v19 offset:9152
	v_cvt_pk_bf16_f32 v19, v95, s0
	ds_write_b16 v18, v19 offset:9216
	v_cvt_pk_bf16_f32 v19, v76, s0
	ds_write_b16 v18, v19 offset:9280
	v_cvt_pk_bf16_f32 v19, v77, s0
	ds_write_b16 v18, v19 offset:9344
	v_cvt_pk_bf16_f32 v19, v78, s0
	ds_write_b16 v18, v19 offset:9408
	v_cvt_pk_bf16_f32 v19, v64, s0
	ds_write_b16 v18, v19 offset:9472
	v_cvt_pk_bf16_f32 v19, v20, s0
	v_fmac_f32_e32 v23, v22, v21
	ds_write_b16 v18, v19 offset:9536
	v_cvt_pk_bf16_f32 v19, v21, s0
	ds_write_b16 v18, v19 offset:9600
	v_cvt_pk_bf16_f32 v19, v23, s0
	ds_write_b16 v18, v19 offset:9664

.LBB0_1734:
	s_mul_i32 s0, s69, 0x3300
	s_add_i32 s0, s74, s0
	s_add_i32 s1, s0, 0x2a00
	v_add_u32_e32 v18, s1, v185
	ds_read_b64_tr_b16 v[20:21], v18
	v_add3_u32 v18, s0, v186, v187
	ds_read2_b64 v[26:29], v18 offset1:4
	ds_read2_b64 v[30:33], v18 offset0:8 offset1:12
	v_add_u32_e32 v18, 0x800, v18
	v_cvt_pk_bf16_f32 v22, v2, v3
	v_cvt_pk_bf16_f32 v23, v4, v5
	v_cvt_pk_bf16_f32 v24, v10, v11
	v_cvt_pk_bf16_f32 v25, v12, v13
	ds_read2_b64 v[38:41], v18 offset0:32 offset1:36
	ds_read2_b64 v[42:45], v18 offset0:40 offset1:44
	s_waitcnt lgkmcnt(3)
	v_mfma_f32_16x16x32_bf16 v[26:29], v[26:29], v[22:25], 0
	s_waitcnt lgkmcnt(0)
	s_add_i32 s76, s69, s68
	v_cvt_pk_bf16_f32 v34, v6, v7
	v_cvt_pk_bf16_f32 v35, v8, v9
	v_cvt_pk_bf16_f32 v36, v14, v15
	v_cvt_pk_bf16_f32 v37, v16, v17
	s_waitcnt lgkmcnt(2)
	s_nop 0
	v_mfma_f32_16x16x32_bf16 v[26:29], v[30:33], v[34:37], v[26:29]
	s_nop 7
	v_cvt_pk_bf16_f32 v18, v26, v27
	v_add_u32_e32 v26, s0, v192
	ds_read_b128 v[30:33], v26 offset:8704
	v_add_u32_e32 v62, s0, v191
	ds_read_b128 v[46:49], v62 offset:12800
	v_cvt_pk_bf16_f32 v19, v28, v29
	ds_read_b128 v[26:29], v26 offset:9728
	ds_read_b128 v[50:53], v62 offset:12864
	v_add_u32_e32 v63, v62, v190
	ds_read_b128 v[54:57], v63 offset:4608
	ds_read_b128 v[58:61], v63 offset:5632
	s_waitcnt lgkmcnt(5)
	v_mfma_f32_16x16x32_bf16 v[30:33], v[30:33], v[18:21], 0
	s_waitcnt lgkmcnt(2)
	v_pk_mul_f32 v[10:11], v[10:11], v[50:51]
	v_pk_mul_f32 v[12:13], v[12:13], v[52:53]
	ds_read_b128 v[50:53], v63 offset:7680
	v_mfma_f32_16x16x32_bf16 v[22:25], v[38:41], v[22:25], 0
	s_nop 2
	v_cvt_pk_bf16_f32 v18, v30, v31
	v_cvt_pk_bf16_f32 v19, v32, v33
	ds_read_b128 v[30:33], v63 offset:6656
	v_pk_mul_f32 v[2:3], v[2:3], v[46:47]
	v_pk_mul_f32 v[4:5], v[4:5], v[48:49]
	ds_read_b128 v[46:49], v62 offset:12928
	v_mfma_f32_16x16x32_bf16 v[22:25], v[42:45], v[34:37], v[22:25]
	s_cmp_lt_u32 s76, 16
	s_waitcnt lgkmcnt(4)
	v_mfma_f32_16x16x32_bf16 v[2:5], v[54:57], v[18:21], v[2:5]
	ds_read_b128 v[54:57], v62 offset:12992
	s_waitcnt lgkmcnt(1)
	v_pk_mul_f32 v[6:7], v[6:7], v[46:47]
	v_pk_mul_f32 v[8:9], v[8:9], v[48:49]
	v_mfma_f32_16x16x32_bf16 v[10:13], v[58:61], v[18:21], v[10:13]
	s_waitcnt lgkmcnt(0)
	v_pk_mul_f32 v[14:15], v[14:15], v[54:55]
	v_pk_mul_f32 v[16:17], v[16:17], v[56:57]
	v_mfma_f32_16x16x32_bf16 v[6:9], v[30:33], v[18:21], v[6:9]
	s_nop 0
	v_mfma_f32_16x16x32_bf16 v[14:17], v[50:53], v[18:21], v[14:17]
	v_mfma_f32_16x16x32_bf16 v[18:21], v[26:29], v[18:21], v[22:25]
	s_cbranch_scc1 .LBB0_1731
	s_nop 1
	v_lshl_or_b32 v24, s76, 4, v184
	v_add_u32_e32 v22, 0xffffff00, v24
	v_sub_u32_e32 v23, 0x40ff, v24
	v_cndmask_b32_e64 v22, v23, v22, s[28:29]
	v_add_u32_e32 v22, s70, v22
	v_ashrrev_i32_e32 v23, 31, v22
	v_lshlrev_b64 v[22:23], 12, v[22:23]
	v_cvt_pk_bf16_f32 v18, v18, s0
	v_lshl_add_u64 v[22:23], v[164:165], 0, v[22:23]
	global_store_short v[22:23], v18, off sc1
	v_add_u32_e32 v18, 0xffffff01, v24
	v_sub_u32_e32 v22, 0x40fe, v24
	v_cndmask_b32_e64 v18, v22, v18, s[28:29]
	v_add_u32_e32 v18, s70, v18
	v_cvt_pk_bf16_f32 v22, v19, s0
	v_ashrrev_i32_e32 v19, 31, v18
	v_lshlrev_b64 v[18:19], 12, v[18:19]
	v_lshl_add_u64 v[18:19], v[164:165], 0, v[18:19]
	global_store_short v[18:19], v22, off sc1
	v_add_u32_e32 v18, 0xffffff02, v24
	v_sub_u32_e32 v19, 0x40fd, v24
	v_cndmask_b32_e64 v18, v19, v18, s[28:29]
	v_add_u32_e32 v18, s70, v18
	v_ashrrev_i32_e32 v19, 31, v18
	v_lshlrev_b64 v[18:19], 12, v[18:19]
	v_cvt_pk_bf16_f32 v20, v20, s0
	v_lshl_add_u64 v[18:19], v[164:165], 0, v[18:19]
	global_store_short v[18:19], v20, off sc1
	v_add_u32_e32 v18, 0xffffff03, v24
	v_sub_u32_e32 v19, 0x40fc, v24
	v_cndmask_b32_e64 v18, v19, v18, s[28:29]
	v_add_u32_e32 v18, s70, v18
	v_ashrrev_i32_e32 v19, 31, v18
	v_lshlrev_b64 v[18:19], 12, v[18:19]
	v_cvt_pk_bf16_f32 v20, v21, s0
	v_lshl_add_u64 v[18:19], v[164:165], 0, v[18:19]
	global_store_short v[18:19], v20, off sc1
	s_branch .LBB0_1731

.Lx14_begin:
	s_mov_b64 exec, -1
	s_cmp_lg_u32 s33, 0x100
	s_cbranch_scc1 .LBB0_1816
	s_waitcnt vmcnt(0) lgkmcnt(0)
	s_barrier
	v_cmp_eq_u32_e32 vcc, 0, v0
	s_and_saveexec_b64 s[98:99], vcc
	s_cbranch_execz .Lx14_sb_done
	buffer_wbl2 sc1
	s_waitcnt vmcnt(0)
	v_mov_b32_e32 v1, 0xc800
	v_mov_b32_e32 v2, 1
	global_atomic_add v1, v2, s[54:55]
	s_waitcnt vmcnt(0)
	s_mov_b32 s0, 0
.Lx14_sb_spin:
	global_load_dword v3, v1, s[54:55] sc1
	s_waitcnt vmcnt(0)
	v_readfirstlane_b32 s1, v3
	s_cmp_ge_u32 s1, 0x80
	s_cbranch_scc1 .Lx14_sb_ok
	s_sleep 4
	s_add_u32 s0, s0, 1
	s_cmp_lt_u32 s0, 0x40000
	s_cbranch_scc1 .Lx14_sb_spin
.Lx14_sb_ok:
	buffer_inv sc1
	s_waitcnt vmcnt(0)
.Lx14_sb_done:
	s_or_b64 exec, exec, s[98:99]
	s_barrier
	v_mbcnt_lo_u32_b32 v1, -1, 0
	v_mbcnt_hi_u32_b32 v1, -1, v1
	v_lshlrev_b32_e32 v2, 4, v1
	v_lshrrev_b32_e32 v3, 3, v1
	v_lshlrev_b32_e32 v3, 2, v3
	v_and_b32_e32 v4, 31, v1
	v_lshlrev_b32_e32 v4, 2, v4
	v_lshrrev_b32_e32 v9, 5, v1
	v_lshl_add_u32 v4, v9, 8, v4
	v_lshlrev_b32_e32 v9, 5, v1
	s_load_dwordx4 s[28:31], s[74:75], 0x100
	s_add_u32 s4, s54, 0x8c00000
	s_addc_u32 s5, s55, 0
	s_add_u32 s6, s54, 0x29400000
	s_addc_u32 s7, s55, 0
	s_add_u32 s8, s54, 0x21200000
	s_addc_u32 s9, s55, 0
	s_add_u32 s10, s54, 0x49c00000
	s_addc_u32 s11, s55, 0
	s_add_u32 s12, s54, 0x19000000
	s_addc_u32 s13, s55, 0
	s_add_u32 s14, s54, 0xc00000
	s_addc_u32 s15, s55, 0
	s_add_u32 s16, s54, 0x1000000
	s_addc_u32 s17, s55, 0
	s_add_u32 s20, s54, 0xc400
	s_addc_u32 s21, s55, 0
	s_mov_b32 s18, -1
	s_mov_b32 s19, 0
	s_add_i32 s25, s2, 0xffffff80
	s_lshl_b32 s25, s25, 3
	s_add_i32 s25, s25, s82
	s_mov_b32 s24, 0
	s_mov_b32 s26, 0
	s_waitcnt lgkmcnt(0)
	global_load_dwordx4 v[10:13], v9, s[28:29]
	global_load_dwordx4 v[14:17], v9, s[28:29] offset:16
	global_load_dwordx4 v[18:21], v9, s[28:29] offset:2048
	global_load_dwordx4 v[22:25], v9, s[28:29] offset:2064
	global_load_dwordx4 v[42:45], v9, s[30:31]
	global_load_dwordx4 v[46:49], v9, s[30:31] offset:16
	global_load_dwordx4 v[50:53], v9, s[30:31] offset:2048
	global_load_dwordx4 v[54:57], v9, s[30:31] offset:2064
	v_add_u32_e32 v9, 0x1000, v9
	global_load_dwordx4 v[26:29], v9, s[28:29]
	global_load_dwordx4 v[30:33], v9, s[28:29] offset:16
	global_load_dwordx4 v[34:37], v9, s[28:29] offset:2048
	global_load_dwordx4 v[38:41], v9, s[28:29] offset:2064
	global_load_dwordx4 v[58:61], v9, s[30:31]
	global_load_dwordx4 v[62:65], v9, s[30:31] offset:16
	global_load_dwordx4 v[66:69], v9, s[30:31] offset:2048
	global_load_dwordx4 v[70:73], v9, s[30:31] offset:2064
	s_waitcnt vmcnt(0)
.Lx14_row:
	s_lshr_b32 s0, s24, 2
	s_lshl_b32 s0, s0, 10
	s_add_i32 s0, s0, s25
	s_and_b32 s1, s24, 1
	s_bfe_u32 s3, s24, 0x10001
	s_sub_i32 s28, 0x1fff, s0
	s_add_i32 s29, s0, 0x2000
	s_cmp_lg_u32 s1, 0
	s_cselect_b32 s28, s29, s28
	s_add_i32 s29, s28, 0x100
	s_lshr_b32 s29, s29, 6
	s_add_i32 s29, s29, 1
	s_sub_i32 s30, 0x40ff, s28
	s_lshr_b32 s30, s30, 6
	s_add_i32 s30, s30, 1
	s_lshl_b32 s31, s3, 14
	s_add_i32 s31, s31, s28
	s_lshl_b32 s3, s3, 7
	v_add_u32_e32 v7, s3, v4
	v_mov_b32_e32 v8, s30
	v_mov_b32_e32 v9, s29
	v_cndmask_b32_e64 v8, v8, v9, s[18:19]
	s_cmp_lg_u32 s26, 0
	s_cbranch_scc1 .Lx14_ready
	s_mov_b32 s27, 0
.Lx14_poll:
	global_load_dword v9, v7, s[20:21] sc1
	s_waitcnt vmcnt(0)
	v_cmp_lt_i32_e32 vcc, v9, v8
	s_cbranch_vccz .Lx14_ready
	s_sleep 8
	s_add_u32 s27, s27, 1
	s_cmp_lt_u32 s27, 0x2000
	s_cbranch_scc1 .Lx14_poll
	s_mov_b32 s26, 1
.Lx14_ready:
	s_lshl_b32 s0, s31, 12
	v_add_u32_e32 v5, s0, v2
	s_lshl_b32 s1, s31, 7
	v_add_u32_e32 v6, s1, v3
	global_load_dwordx4 v[80:83], v5, s[4:5] sc1
	global_load_dwordx4 v[84:87], v5, s[4:5] offset:1024 sc1
	global_load_dwordx4 v[88:91], v5, s[4:5] offset:2048 sc1
	global_load_dwordx4 v[92:95], v5, s[4:5] offset:3072 sc1
	global_load_dwordx4 v[96:99], v5, s[6:7] sc1
	global_load_dwordx4 v[100:103], v5, s[6:7] offset:1024 sc1
	global_load_dwordx4 v[104:107], v5, s[6:7] offset:2048 sc1
	global_load_dwordx4 v[108:111], v5, s[6:7] offset:3072 sc1
	global_load_dwordx4 v[112:115], v5, s[8:9]
	global_load_dwordx4 v[116:119], v5, s[8:9] offset:1024
	global_load_dwordx4 v[120:123], v5, s[8:9] offset:2048
	global_load_dwordx4 v[124:127], v5, s[8:9] offset:3072
	global_load_dwordx4 v[128:131], v5, s[10:11]
	global_load_dwordx4 v[132:135], v5, s[10:11] offset:1024
	global_load_dwordx4 v[136:139], v5, s[10:11] offset:2048
	global_load_dwordx4 v[140:143], v5, s[10:11] offset:3072
	global_load_dword v144, v6, s[14:15]
	global_load_dword v145, v6, s[14:15] offset:32
	global_load_dword v146, v6, s[14:15] offset:64
	global_load_dword v147, v6, s[14:15] offset:96
	global_load_dword v148, v6, s[16:17]
	global_load_dword v149, v6, s[16:17] offset:32
	global_load_dword v150, v6, s[16:17] offset:64
	global_load_dword v151, v6, s[16:17] offset:96
	s_waitcnt vmcnt(0)
	v_lshlrev_b32_e32 v168, 16, v80
	v_lshlrev_b32_e32 v169, 16, v96
	v_add_f32_e32 v160, v168, v169
	v_and_b32_e32 v168, 0xffff0000, v80
	v_and_b32_e32 v169, 0xffff0000, v96
	v_add_f32_e32 v161, v168, v169
	v_lshlrev_b32_e32 v168, 16, v81
	v_lshlrev_b32_e32 v169, 16, v97
	v_add_f32_e32 v162, v168, v169
	v_and_b32_e32 v168, 0xffff0000, v81
	v_and_b32_e32 v169, 0xffff0000, v97
	v_add_f32_e32 v163, v168, v169
	v_lshlrev_b32_e32 v168, 16, v82
	v_lshlrev_b32_e32 v169, 16, v98
	v_add_f32_e32 v164, v168, v169
	v_and_b32_e32 v168, 0xffff0000, v82
	v_and_b32_e32 v169, 0xffff0000, v98
	v_add_f32_e32 v165, v168, v169
	v_lshlrev_b32_e32 v168, 16, v83
	v_lshlrev_b32_e32 v169, 16, v99
	v_add_f32_e32 v166, v168, v169
	v_and_b32_e32 v168, 0xffff0000, v83
	v_and_b32_e32 v169, 0xffff0000, v99
	v_add_f32_e32 v167, v168, v169
	v_add_f32_e32 v170, v160, v161
	v_add_f32_e32 v170, v170, v162
	v_add_f32_e32 v170, v170, v163
	v_add_f32_e32 v170, v170, v164
	v_add_f32_e32 v170, v170, v165
	v_add_f32_e32 v170, v170, v166
	v_add_f32_e32 v170, v170, v167
	s_nop 1
	v_add_f32_dpp v170, v170, v170 quad_perm:[1,0,3,2] row_mask:0xf bank_mask:0xf bound_ctrl:1
	s_nop 1
	v_add_f32_dpp v170, v170, v170 quad_perm:[2,3,0,1] row_mask:0xf bank_mask:0xf bound_ctrl:1
	s_nop 1
	v_add_f32_dpp v170, v170, v170 row_half_mirror row_mask:0xf bank_mask:0xf bound_ctrl:1
	v_mul_f32_e32 v170, 0x3c800000, v170
	v_sub_f32_e32 v160, v160, v170
	v_sub_f32_e32 v161, v161, v170
	v_sub_f32_e32 v162, v162, v170
	v_sub_f32_e32 v163, v163, v170
	v_sub_f32_e32 v164, v164, v170
	v_sub_f32_e32 v165, v165, v170
	v_sub_f32_e32 v166, v166, v170
	v_sub_f32_e32 v167, v167, v170
	v_mul_f32_e32 v171, v160, v160
	v_fmac_f32_e32 v171, v161, v161
	v_fmac_f32_e32 v171, v162, v162
	v_fmac_f32_e32 v171, v163, v163
	v_fmac_f32_e32 v171, v164, v164
	v_fmac_f32_e32 v171, v165, v165
	v_fmac_f32_e32 v171, v166, v166
	v_fmac_f32_e32 v171, v167, v167
	s_nop 1
	v_add_f32_dpp v171, v171, v171 quad_perm:[1,0,3,2] row_mask:0xf bank_mask:0xf bound_ctrl:1
	s_nop 1
	v_add_f32_dpp v171, v171, v171 quad_perm:[2,3,0,1] row_mask:0xf bank_mask:0xf bound_ctrl:1
	s_nop 1
	v_add_f32_dpp v171, v171, v171 row_half_mirror row_mask:0xf bank_mask:0xf bound_ctrl:1
	v_mov_b32_e32 v172, 0x3a27c5ac
	v_fmac_f32_e32 v172, 0x3c800000, v171
	v_rsq_f32_e32 v172, v172
	v_add_f32_e32 v173, v144, v148
	s_nop 0
	v_mul_f32_e32 v160, v160, v172
	v_mul_f32_e32 v161, v161, v172
	v_mul_f32_e32 v162, v162, v172
	v_mul_f32_e32 v163, v163, v172
	v_mul_f32_e32 v164, v164, v172
	v_mul_f32_e32 v165, v165, v172
	v_mul_f32_e32 v166, v166, v172
	v_mul_f32_e32 v167, v167, v172
	v_fma_f32 v160, v10, v160, v42
	v_fma_f32 v161, v11, v161, v43
	v_fma_f32 v162, v12, v162, v44
	v_fma_f32 v163, v13, v163, v45
	v_fma_f32 v164, v14, v164, v46
	v_fma_f32 v165, v15, v165, v47
	v_fma_f32 v166, v16, v166, v48
	v_fma_f32 v167, v17, v167, v49
	v_lshlrev_b32_e32 v168, 16, v112
	v_fmac_f32_e32 v160, v173, v168
	v_and_b32_e32 v169, 0xffff0000, v112
	v_fmac_f32_e32 v161, v173, v169
	v_lshlrev_b32_e32 v168, 16, v128
	v_mul_f32_e32 v160, v160, v168
	v_and_b32_e32 v169, 0xffff0000, v128
	v_mul_f32_e32 v161, v161, v169
	v_lshlrev_b32_e32 v168, 16, v113
	v_fmac_f32_e32 v162, v173, v168
	v_and_b32_e32 v169, 0xffff0000, v113
	v_fmac_f32_e32 v163, v173, v169
	v_lshlrev_b32_e32 v168, 16, v129
	v_mul_f32_e32 v162, v162, v168
	v_and_b32_e32 v169, 0xffff0000, v129
	v_mul_f32_e32 v163, v163, v169
	v_lshlrev_b32_e32 v168, 16, v114
	v_fmac_f32_e32 v164, v173, v168
	v_and_b32_e32 v169, 0xffff0000, v114
	v_fmac_f32_e32 v165, v173, v169
	v_lshlrev_b32_e32 v168, 16, v130
	v_mul_f32_e32 v164, v164, v168
	v_and_b32_e32 v169, 0xffff0000, v130
	v_mul_f32_e32 v165, v165, v169
	v_lshlrev_b32_e32 v168, 16, v115
	v_fmac_f32_e32 v166, v173, v168
	v_and_b32_e32 v169, 0xffff0000, v115
	v_fmac_f32_e32 v167, v173, v169
	v_lshlrev_b32_e32 v168, 16, v131
	v_mul_f32_e32 v166, v166, v168
	v_and_b32_e32 v169, 0xffff0000, v131
	v_mul_f32_e32 v167, v167, v169
	v_cvt_pk_bf16_f32 v180, v160, v161
	v_cvt_pk_bf16_f32 v181, v162, v163
	v_cvt_pk_bf16_f32 v182, v164, v165
	v_cvt_pk_bf16_f32 v183, v166, v167
	global_store_dwordx4 v5, v[180:183], s[12:13]
	v_lshlrev_b32_e32 v168, 16, v84
	v_lshlrev_b32_e32 v169, 16, v100
	v_add_f32_e32 v160, v168, v169
	v_and_b32_e32 v168, 0xffff0000, v84
	v_and_b32_e32 v169, 0xffff0000, v100
	v_add_f32_e32 v161, v168, v169
	v_lshlrev_b32_e32 v168, 16, v85
	v_lshlrev_b32_e32 v169, 16, v101
	v_add_f32_e32 v162, v168, v169
	v_and_b32_e32 v168, 0xffff0000, v85
	v_and_b32_e32 v169, 0xffff0000, v101
	v_add_f32_e32 v163, v168, v169
	v_lshlrev_b32_e32 v168, 16, v86
	v_lshlrev_b32_e32 v169, 16, v102
	v_add_f32_e32 v164, v168, v169
	v_and_b32_e32 v168, 0xffff0000, v86
	v_and_b32_e32 v169, 0xffff0000, v102
	v_add_f32_e32 v165, v168, v169
	v_lshlrev_b32_e32 v168, 16, v87
	v_lshlrev_b32_e32 v169, 16, v103
	v_add_f32_e32 v166, v168, v169
	v_and_b32_e32 v168, 0xffff0000, v87
	v_and_b32_e32 v169, 0xffff0000, v103
	v_add_f32_e32 v167, v168, v169
	v_add_f32_e32 v170, v160, v161
	v_add_f32_e32 v170, v170, v162
	v_add_f32_e32 v170, v170, v163
	v_add_f32_e32 v170, v170, v164
	v_add_f32_e32 v170, v170, v165
	v_add_f32_e32 v170, v170, v166
	v_add_f32_e32 v170, v170, v167
	s_nop 1
	v_add_f32_dpp v170, v170, v170 quad_perm:[1,0,3,2] row_mask:0xf bank_mask:0xf bound_ctrl:1
	s_nop 1
	v_add_f32_dpp v170, v170, v170 quad_perm:[2,3,0,1] row_mask:0xf bank_mask:0xf bound_ctrl:1
	s_nop 1
	v_add_f32_dpp v170, v170, v170 row_half_mirror row_mask:0xf bank_mask:0xf bound_ctrl:1
	v_mul_f32_e32 v170, 0x3c800000, v170
	v_sub_f32_e32 v160, v160, v170
	v_sub_f32_e32 v161, v161, v170
	v_sub_f32_e32 v162, v162, v170
	v_sub_f32_e32 v163, v163, v170
	v_sub_f32_e32 v164, v164, v170
	v_sub_f32_e32 v165, v165, v170
	v_sub_f32_e32 v166, v166, v170
	v_sub_f32_e32 v167, v167, v170
	v_mul_f32_e32 v171, v160, v160
	v_fmac_f32_e32 v171, v161, v161
	v_fmac_f32_e32 v171, v162, v162
	v_fmac_f32_e32 v171, v163, v163
	v_fmac_f32_e32 v171, v164, v164
	v_fmac_f32_e32 v171, v165, v165
	v_fmac_f32_e32 v171, v166, v166
	v_fmac_f32_e32 v171, v167, v167
	s_nop 1
	v_add_f32_dpp v171, v171, v171 quad_perm:[1,0,3,2] row_mask:0xf bank_mask:0xf bound_ctrl:1
	s_nop 1
	v_add_f32_dpp v171, v171, v171 quad_perm:[2,3,0,1] row_mask:0xf bank_mask:0xf bound_ctrl:1
	s_nop 1
	v_add_f32_dpp v171, v171, v171 row_half_mirror row_mask:0xf bank_mask:0xf bound_ctrl:1
	v_mov_b32_e32 v172, 0x3a27c5ac
	v_fmac_f32_e32 v172, 0x3c800000, v171
	v_rsq_f32_e32 v172, v172
	v_add_f32_e32 v173, v145, v149
	s_nop 0
	v_mul_f32_e32 v160, v160, v172
	v_mul_f32_e32 v161, v161, v172
	v_mul_f32_e32 v162, v162, v172
	v_mul_f32_e32 v163, v163, v172
	v_mul_f32_e32 v164, v164, v172
	v_mul_f32_e32 v165, v165, v172
	v_mul_f32_e32 v166, v166, v172
	v_mul_f32_e32 v167, v167, v172
	v_fma_f32 v160, v18, v160, v50
	v_fma_f32 v161, v19, v161, v51
	v_fma_f32 v162, v20, v162, v52
	v_fma_f32 v163, v21, v163, v53
	v_fma_f32 v164, v22, v164, v54
	v_fma_f32 v165, v23, v165, v55
	v_fma_f32 v166, v24, v166, v56
	v_fma_f32 v167, v25, v167, v57
	v_lshlrev_b32_e32 v168, 16, v116
	v_fmac_f32_e32 v160, v173, v168
	v_and_b32_e32 v169, 0xffff0000, v116
	v_fmac_f32_e32 v161, v173, v169
	v_lshlrev_b32_e32 v168, 16, v132
	v_mul_f32_e32 v160, v160, v168
	v_and_b32_e32 v169, 0xffff0000, v132
	v_mul_f32_e32 v161, v161, v169
	v_lshlrev_b32_e32 v168, 16, v117
	v_fmac_f32_e32 v162, v173, v168
	v_and_b32_e32 v169, 0xffff0000, v117
	v_fmac_f32_e32 v163, v173, v169
	v_lshlrev_b32_e32 v168, 16, v133
	v_mul_f32_e32 v162, v162, v168
	v_and_b32_e32 v169, 0xffff0000, v133
	v_mul_f32_e32 v163, v163, v169
	v_lshlrev_b32_e32 v168, 16, v118
	v_fmac_f32_e32 v164, v173, v168
	v_and_b32_e32 v169, 0xffff0000, v118
	v_fmac_f32_e32 v165, v173, v169
	v_lshlrev_b32_e32 v168, 16, v134
	v_mul_f32_e32 v164, v164, v168
	v_and_b32_e32 v169, 0xffff0000, v134
	v_mul_f32_e32 v165, v165, v169
	v_lshlrev_b32_e32 v168, 16, v119
	v_fmac_f32_e32 v166, v173, v168
	v_and_b32_e32 v169, 0xffff0000, v119
	v_fmac_f32_e32 v167, v173, v169
	v_lshlrev_b32_e32 v168, 16, v135
	v_mul_f32_e32 v166, v166, v168
	v_and_b32_e32 v169, 0xffff0000, v135
	v_mul_f32_e32 v167, v167, v169
	v_cvt_pk_bf16_f32 v184, v160, v161
	v_cvt_pk_bf16_f32 v185, v162, v163
	v_cvt_pk_bf16_f32 v186, v164, v165
	v_cvt_pk_bf16_f32 v187, v166, v167
	global_store_dwordx4 v5, v[184:187], s[12:13] offset:1024
	v_lshlrev_b32_e32 v168, 16, v88
	v_lshlrev_b32_e32 v169, 16, v104
	v_add_f32_e32 v160, v168, v169
	v_and_b32_e32 v168, 0xffff0000, v88
	v_and_b32_e32 v169, 0xffff0000, v104
	v_add_f32_e32 v161, v168, v169
	v_lshlrev_b32_e32 v168, 16, v89
	v_lshlrev_b32_e32 v169, 16, v105
	v_add_f32_e32 v162, v168, v169
	v_and_b32_e32 v168, 0xffff0000, v89
	v_and_b32_e32 v169, 0xffff0000, v105
	v_add_f32_e32 v163, v168, v169
	v_lshlrev_b32_e32 v168, 16, v90
	v_lshlrev_b32_e32 v169, 16, v106
	v_add_f32_e32 v164, v168, v169
	v_and_b32_e32 v168, 0xffff0000, v90
	v_and_b32_e32 v169, 0xffff0000, v106
	v_add_f32_e32 v165, v168, v169
	v_lshlrev_b32_e32 v168, 16, v91
	v_lshlrev_b32_e32 v169, 16, v107
	v_add_f32_e32 v166, v168, v169
	v_and_b32_e32 v168, 0xffff0000, v91
	v_and_b32_e32 v169, 0xffff0000, v107
	v_add_f32_e32 v167, v168, v169
	v_add_f32_e32 v170, v160, v161
	v_add_f32_e32 v170, v170, v162
	v_add_f32_e32 v170, v170, v163
	v_add_f32_e32 v170, v170, v164
	v_add_f32_e32 v170, v170, v165
	v_add_f32_e32 v170, v170, v166
	v_add_f32_e32 v170, v170, v167
	s_nop 1
	v_add_f32_dpp v170, v170, v170 quad_perm:[1,0,3,2] row_mask:0xf bank_mask:0xf bound_ctrl:1
	s_nop 1
	v_add_f32_dpp v170, v170, v170 quad_perm:[2,3,0,1] row_mask:0xf bank_mask:0xf bound_ctrl:1
	s_nop 1
	v_add_f32_dpp v170, v170, v170 row_half_mirror row_mask:0xf bank_mask:0xf bound_ctrl:1
	v_mul_f32_e32 v170, 0x3c800000, v170
	v_sub_f32_e32 v160, v160, v170
	v_sub_f32_e32 v161, v161, v170
	v_sub_f32_e32 v162, v162, v170
	v_sub_f32_e32 v163, v163, v170
	v_sub_f32_e32 v164, v164, v170
	v_sub_f32_e32 v165, v165, v170
	v_sub_f32_e32 v166, v166, v170
	v_sub_f32_e32 v167, v167, v170
	v_mul_f32_e32 v171, v160, v160
	v_fmac_f32_e32 v171, v161, v161
	v_fmac_f32_e32 v171, v162, v162
	v_fmac_f32_e32 v171, v163, v163
	v_fmac_f32_e32 v171, v164, v164
	v_fmac_f32_e32 v171, v165, v165
	v_fmac_f32_e32 v171, v166, v166
	v_fmac_f32_e32 v171, v167, v167
	s_nop 1
	v_add_f32_dpp v171, v171, v171 quad_perm:[1,0,3,2] row_mask:0xf bank_mask:0xf bound_ctrl:1
	s_nop 1
	v_add_f32_dpp v171, v171, v171 quad_perm:[2,3,0,1] row_mask:0xf bank_mask:0xf bound_ctrl:1
	s_nop 1
	v_add_f32_dpp v171, v171, v171 row_half_mirror row_mask:0xf bank_mask:0xf bound_ctrl:1
	v_mov_b32_e32 v172, 0x3a27c5ac
	v_fmac_f32_e32 v172, 0x3c800000, v171
	v_rsq_f32_e32 v172, v172
	v_add_f32_e32 v173, v146, v150
	s_nop 0
	v_mul_f32_e32 v160, v160, v172
	v_mul_f32_e32 v161, v161, v172
	v_mul_f32_e32 v162, v162, v172
	v_mul_f32_e32 v163, v163, v172
	v_mul_f32_e32 v164, v164, v172
	v_mul_f32_e32 v165, v165, v172
	v_mul_f32_e32 v166, v166, v172
	v_mul_f32_e32 v167, v167, v172
	v_fma_f32 v160, v26, v160, v58
	v_fma_f32 v161, v27, v161, v59
	v_fma_f32 v162, v28, v162, v60
	v_fma_f32 v163, v29, v163, v61
	v_fma_f32 v164, v30, v164, v62
	v_fma_f32 v165, v31, v165, v63
	v_fma_f32 v166, v32, v166, v64
	v_fma_f32 v167, v33, v167, v65
	v_lshlrev_b32_e32 v168, 16, v120
	v_fmac_f32_e32 v160, v173, v168
	v_and_b32_e32 v169, 0xffff0000, v120
	v_fmac_f32_e32 v161, v173, v169
	v_lshlrev_b32_e32 v168, 16, v136
	v_mul_f32_e32 v160, v160, v168
	v_and_b32_e32 v169, 0xffff0000, v136
	v_mul_f32_e32 v161, v161, v169
	v_lshlrev_b32_e32 v168, 16, v121
	v_fmac_f32_e32 v162, v173, v168
	v_and_b32_e32 v169, 0xffff0000, v121
	v_fmac_f32_e32 v163, v173, v169
	v_lshlrev_b32_e32 v168, 16, v137
	v_mul_f32_e32 v162, v162, v168
	v_and_b32_e32 v169, 0xffff0000, v137
	v_mul_f32_e32 v163, v163, v169
	v_lshlrev_b32_e32 v168, 16, v122
	v_fmac_f32_e32 v164, v173, v168
	v_and_b32_e32 v169, 0xffff0000, v122
	v_fmac_f32_e32 v165, v173, v169
	v_lshlrev_b32_e32 v168, 16, v138
	v_mul_f32_e32 v164, v164, v168
	v_and_b32_e32 v169, 0xffff0000, v138
	v_mul_f32_e32 v165, v165, v169
	v_lshlrev_b32_e32 v168, 16, v123
	v_fmac_f32_e32 v166, v173, v168
	v_and_b32_e32 v169, 0xffff0000, v123
	v_fmac_f32_e32 v167, v173, v169
	v_lshlrev_b32_e32 v168, 16, v139
	v_mul_f32_e32 v166, v166, v168
	v_and_b32_e32 v169, 0xffff0000, v139
	v_mul_f32_e32 v167, v167, v169
	v_cvt_pk_bf16_f32 v192, v160, v161
	v_cvt_pk_bf16_f32 v193, v162, v163
	v_cvt_pk_bf16_f32 v194, v164, v165
	v_cvt_pk_bf16_f32 v195, v166, v167
	global_store_dwordx4 v5, v[192:195], s[12:13] offset:2048
	v_lshlrev_b32_e32 v168, 16, v92
	v_lshlrev_b32_e32 v169, 16, v108
	v_add_f32_e32 v160, v168, v169
	v_and_b32_e32 v168, 0xffff0000, v92
	v_and_b32_e32 v169, 0xffff0000, v108
	v_add_f32_e32 v161, v168, v169
	v_lshlrev_b32_e32 v168, 16, v93
	v_lshlrev_b32_e32 v169, 16, v109
	v_add_f32_e32 v162, v168, v169
	v_and_b32_e32 v168, 0xffff0000, v93
	v_and_b32_e32 v169, 0xffff0000, v109
	v_add_f32_e32 v163, v168, v169
	v_lshlrev_b32_e32 v168, 16, v94
	v_lshlrev_b32_e32 v169, 16, v110
	v_add_f32_e32 v164, v168, v169
	v_and_b32_e32 v168, 0xffff0000, v94
	v_and_b32_e32 v169, 0xffff0000, v110
	v_add_f32_e32 v165, v168, v169
	v_lshlrev_b32_e32 v168, 16, v95
	v_lshlrev_b32_e32 v169, 16, v111
	v_add_f32_e32 v166, v168, v169
	v_and_b32_e32 v168, 0xffff0000, v95
	v_and_b32_e32 v169, 0xffff0000, v111
	v_add_f32_e32 v167, v168, v169
	v_add_f32_e32 v170, v160, v161
	v_add_f32_e32 v170, v170, v162
	v_add_f32_e32 v170, v170, v163
	v_add_f32_e32 v170, v170, v164
	v_add_f32_e32 v170, v170, v165
	v_add_f32_e32 v170, v170, v166
	v_add_f32_e32 v170, v170, v167
	s_nop 1
	v_add_f32_dpp v170, v170, v170 quad_perm:[1,0,3,2] row_mask:0xf bank_mask:0xf bound_ctrl:1
	s_nop 1
	v_add_f32_dpp v170, v170, v170 quad_perm:[2,3,0,1] row_mask:0xf bank_mask:0xf bound_ctrl:1
	s_nop 1
	v_add_f32_dpp v170, v170, v170 row_half_mirror row_mask:0xf bank_mask:0xf bound_ctrl:1
	v_mul_f32_e32 v170, 0x3c800000, v170
	v_sub_f32_e32 v160, v160, v170
	v_sub_f32_e32 v161, v161, v170
	v_sub_f32_e32 v162, v162, v170
	v_sub_f32_e32 v163, v163, v170
	v_sub_f32_e32 v164, v164, v170
	v_sub_f32_e32 v165, v165, v170
	v_sub_f32_e32 v166, v166, v170
	v_sub_f32_e32 v167, v167, v170
	v_mul_f32_e32 v171, v160, v160
	v_fmac_f32_e32 v171, v161, v161
	v_fmac_f32_e32 v171, v162, v162
	v_fmac_f32_e32 v171, v163, v163
	v_fmac_f32_e32 v171, v164, v164
	v_fmac_f32_e32 v171, v165, v165
	v_fmac_f32_e32 v171, v166, v166
	v_fmac_f32_e32 v171, v167, v167
	s_nop 1
	v_add_f32_dpp v171, v171, v171 quad_perm:[1,0,3,2] row_mask:0xf bank_mask:0xf bound_ctrl:1
	s_nop 1
	v_add_f32_dpp v171, v171, v171 quad_perm:[2,3,0,1] row_mask:0xf bank_mask:0xf bound_ctrl:1
	s_nop 1
	v_add_f32_dpp v171, v171, v171 row_half_mirror row_mask:0xf bank_mask:0xf bound_ctrl:1
	v_mov_b32_e32 v172, 0x3a27c5ac
	v_fmac_f32_e32 v172, 0x3c800000, v171
	v_rsq_f32_e32 v172, v172
	v_add_f32_e32 v173, v147, v151
	s_nop 0
	v_mul_f32_e32 v160, v160, v172
	v_mul_f32_e32 v161, v161, v172
	v_mul_f32_e32 v162, v162, v172
	v_mul_f32_e32 v163, v163, v172
	v_mul_f32_e32 v164, v164, v172
	v_mul_f32_e32 v165, v165, v172
	v_mul_f32_e32 v166, v166, v172
	v_mul_f32_e32 v167, v167, v172
	v_fma_f32 v160, v34, v160, v66
	v_fma_f32 v161, v35, v161, v67
	v_fma_f32 v162, v36, v162, v68
	v_fma_f32 v163, v37, v163, v69
	v_fma_f32 v164, v38, v164, v70
	v_fma_f32 v165, v39, v165, v71
	v_fma_f32 v166, v40, v166, v72
	v_fma_f32 v167, v41, v167, v73
	v_lshlrev_b32_e32 v168, 16, v124
	v_fmac_f32_e32 v160, v173, v168
	v_and_b32_e32 v169, 0xffff0000, v124
	v_fmac_f32_e32 v161, v173, v169
	v_lshlrev_b32_e32 v168, 16, v140
	v_mul_f32_e32 v160, v160, v168
	v_and_b32_e32 v169, 0xffff0000, v140
	v_mul_f32_e32 v161, v161, v169
	v_lshlrev_b32_e32 v168, 16, v125
	v_fmac_f32_e32 v162, v173, v168
	v_and_b32_e32 v169, 0xffff0000, v125
	v_fmac_f32_e32 v163, v173, v169
	v_lshlrev_b32_e32 v168, 16, v141
	v_mul_f32_e32 v162, v162, v168
	v_and_b32_e32 v169, 0xffff0000, v141
	v_mul_f32_e32 v163, v163, v169
	v_lshlrev_b32_e32 v168, 16, v126
	v_fmac_f32_e32 v164, v173, v168
	v_and_b32_e32 v169, 0xffff0000, v126
	v_fmac_f32_e32 v165, v173, v169
	v_lshlrev_b32_e32 v168, 16, v142
	v_mul_f32_e32 v164, v164, v168
	v_and_b32_e32 v169, 0xffff0000, v142
	v_mul_f32_e32 v165, v165, v169
	v_lshlrev_b32_e32 v168, 16, v127
	v_fmac_f32_e32 v166, v173, v168
	v_and_b32_e32 v169, 0xffff0000, v127
	v_fmac_f32_e32 v167, v173, v169
	v_lshlrev_b32_e32 v168, 16, v143
	v_mul_f32_e32 v166, v166, v168
	v_and_b32_e32 v169, 0xffff0000, v143
	v_mul_f32_e32 v167, v167, v169
	v_cvt_pk_bf16_f32 v196, v160, v161
	v_cvt_pk_bf16_f32 v197, v162, v163
	v_cvt_pk_bf16_f32 v198, v164, v165
	v_cvt_pk_bf16_f32 v199, v166, v167
	global_store_dwordx4 v5, v[196:199], s[12:13] offset:3072
	s_add_i32 s24, s24, 1
	s_cmp_lt_u32 s24, 32
	s_cbranch_scc1 .Lx14_row

.LBB0_1866:
	s_cmp_eq_u32 s33, 0x100
	s_cbranch_scc1 .LBB0_1872
	s_cmp_lt_i32 s72, 15
	s_cselect_b64 s[4:5], -1, 0
	s_and_b64 s[0:1], s[4:5], s[6:7]
	s_andn2_b64 vcc, exec, s[0:1]
	s_cbranch_vccnz .LBB0_1872
	s_lshl_b32 s0, s2, 3
	s_add_i32 s6, s82, s0
	s_cmpk_gt_i32 s6, 0x7fff
	s_cbranch_scc1 .LBB0_1872
	s_add_u32 s0, s54, 0x8c00000
	s_addc_u32 s1, s55, 0
	s_add_u32 s8, s54, 0x29400000
	s_addc_u32 s9, s55, 0
	s_add_u32 s10, s54, 0x21200000
	s_addc_u32 s11, s55, 0
	s_add_u32 s12, s54, 0x49c00000
	s_addc_u32 s13, s55, 0
	v_and_b32_e32 v1, 63, v0
	s_ashr_i32 s7, s6, 31
	s_lshl_b64 s[14:15], s[6:7], 12
	v_lshlrev_b32_e32 v22, 4, v1
	v_or_b32_e32 v146, s14, v22
	v_mov_b32_e32 v147, s15
	v_lshl_add_u64 v[2:3], s[0:1], 0, v[146:147]
	v_lshl_add_u64 v[4:5], s[8:9], 0, v[146:147]
	global_load_dwordx4 v[126:129], v[2:3], off
	global_load_dwordx4 v[122:125], v[4:5], off
	v_lshl_add_u64 v[2:3], s[10:11], 0, v[146:147]
	v_lshl_add_u64 v[4:5], s[12:13], 0, v[146:147]
	global_load_dwordx4 v[118:121], v[2:3], off
	global_load_dwordx4 v[106:109], v[4:5], off
	v_or_b32_e32 v2, 0x400, v146
	v_mov_b32_e32 v3, s15
	v_lshl_add_u64 v[4:5], s[0:1], 0, v[2:3]
	v_lshl_add_u64 v[6:7], s[8:9], 0, v[2:3]
	global_load_dwordx4 v[114:117], v[4:5], off
	global_load_dwordx4 v[110:113], v[6:7], off
	v_lshl_add_u64 v[4:5], s[10:11], 0, v[2:3]
	v_lshl_add_u64 v[2:3], s[12:13], 0, v[2:3]
	global_load_dwordx4 v[102:105], v[4:5], off
	global_load_dwordx4 v[98:101], v[2:3], off
	v_or_b32_e32 v2, 0x800, v146
	v_mov_b32_e32 v3, s15
	v_lshl_add_u64 v[4:5], s[0:1], 0, v[2:3]
	v_lshl_add_u64 v[6:7], s[8:9], 0, v[2:3]
	global_load_dwordx4 v[94:97], v[4:5], off
	global_load_dwordx4 v[90:93], v[6:7], off
	v_lshl_add_u64 v[4:5], s[10:11], 0, v[2:3]
	v_lshl_add_u64 v[2:3], s[12:13], 0, v[2:3]
	global_load_dwordx4 v[14:17], v[4:5], off
	global_load_dwordx4 v[10:13], v[2:3], off
	v_or_b32_e32 v2, 0xc00, v146
	v_mov_b32_e32 v3, s15
	v_lshl_add_u64 v[4:5], s[0:1], 0, v[2:3]
	v_lshl_add_u64 v[6:7], s[8:9], 0, v[2:3]
	v_lshl_add_u64 v[18:19], s[10:11], 0, v[2:3]
	global_load_dwordx4 v[86:89], v[4:5], off
	global_load_dwordx4 v[82:85], v[6:7], off
	v_lshl_add_u64 v[20:21], s[12:13], 0, v[2:3]
	global_load_dwordx4 v[6:9], v[18:19], off
	global_load_dwordx4 v[2:5], v[20:21], off
	s_load_dwordx4 s[12:15], s[74:75], 0x100
	s_lshl_b32 s8, s33, 3
	v_lshlrev_b32_e32 v18, 5, v1
	s_lshl_b64 s[0:1], s[6:7], 7
	v_lshrrev_b32_e32 v1, 1, v0
	v_and_or_b32 v160, v1, 28, s0
	s_add_i32 s0, s6, s8
	v_mov_b32_e32 v19, 0
	v_mov_b32_e32 v161, s1
	s_ashr_i32 s1, s0, 31
	s_waitcnt lgkmcnt(0)
	v_lshl_add_u64 v[148:149], s[12:13], 0, v[18:19]
	v_lshl_add_u64 v[150:151], s[14:15], 0, v[18:19]
	v_or_b32_e32 v20, 0x1000, v18
	v_mov_b32_e32 v21, v19
	v_or_b32_e32 v18, 0x1800, v18
	s_ashr_i32 s9, s8, 31
	s_lshl_b64 s[0:1], s[0:1], 12
	v_lshl_add_u64 v[152:153], s[12:13], 0, v[20:21]
	v_lshl_add_u64 v[154:155], s[14:15], 0, v[20:21]
	v_lshl_add_u64 v[156:157], s[12:13], 0, v[18:19]
	v_lshl_add_u64 v[158:159], s[14:15], 0, v[18:19]
	s_lshl_b64 s[10:11], s[8:9], 12
	s_lshl_b64 s[12:13], s[8:9], 7
	v_or_b32_e32 v162, s0, v22
	v_mov_b32_e32 v163, s1
	s_mov_b32 s3, 0xc00000
	s_mov_b32 s7, 0x1000000
	s_mov_b32 s14, 0x3c800000
	s_mov_b32 s16, 0x3a27c5ac
	s_mov_b32 s9, 0x800000
	s_mov_b32 s15, 0x19000000
	s_branch .LBB0_1870

	.amdhsa_kernel _Z3fwd4Args
		.amdhsa_group_segment_fixed_size 0
		.amdhsa_private_segment_fixed_size 0
		.amdhsa_kernarg_size 592
		.amdhsa_user_sgpr_count 2
		.amdhsa_user_sgpr_dispatch_ptr 0
		.amdhsa_user_sgpr_queue_ptr 0
		.amdhsa_user_sgpr_kernarg_segment_ptr 1
		.amdhsa_user_sgpr_dispatch_id 0
		.amdhsa_user_sgpr_kernarg_preload_length 0
		.amdhsa_user_sgpr_kernarg_preload_offset 0
		.amdhsa_user_sgpr_private_segment_size 0
		.amdhsa_uses_dynamic_stack 0
		.amdhsa_enable_private_segment 0
		.amdhsa_system_sgpr_workgroup_id_x 1
		.amdhsa_system_sgpr_workgroup_id_y 0
		.amdhsa_system_sgpr_workgroup_id_z 0
		.amdhsa_system_sgpr_workgroup_info 0
		.amdhsa_system_vgpr_workitem_id 0
		.amdhsa_next_free_vgpr 256
		.amdhsa_next_free_sgpr 102
		.amdhsa_accum_offset 256
		.amdhsa_reserve_vcc 1
		.amdhsa_float_round_mode_32 0
		.amdhsa_float_round_mode_16_64 0
		.amdhsa_float_denorm_mode_32 3
		.amdhsa_float_denorm_mode_16_64 3
		.amdhsa_dx10_clamp 1
		.amdhsa_ieee_mode 1
		.amdhsa_fp16_overflow 0
		.amdhsa_tg_split 0
		.amdhsa_exception_fp_ieee_invalid_op 0
		.amdhsa_exception_fp_denorm_src 0
		.amdhsa_exception_fp_ieee_div_zero 0
		.amdhsa_exception_fp_ieee_overflow 0
		.amdhsa_exception_fp_ieee_underflow 0
		.amdhsa_exception_fp_ieee_inexact 0
		.amdhsa_exception_int_div_zero 0
	.end_amdhsa_kernel

amdhsa.kernels:
  - .agpr_count:     0
    .args:
      - .offset:         0
        .size:           336
        .value_kind:     by_value
      - .offset:         336
        .size:           4
        .value_kind:     hidden_block_count_x
      - .offset:         340
        .size:           4
        .value_kind:     hidden_block_count_y
      - .offset:         344
        .size:           4
        .value_kind:     hidden_block_count_z
      - .offset:         348
        .size:           2
        .value_kind:     hidden_group_size_x
      - .offset:         350
        .size:           2
        .value_kind:     hidden_group_size_y
      - .offset:         352
        .size:           2
        .value_kind:     hidden_group_size_z
      - .offset:         354
        .size:           2
        .value_kind:     hidden_remainder_x
      - .offset:         356
        .size:           2
        .value_kind:     hidden_remainder_y
      - .offset:         358
        .size:           2
        .value_kind:     hidden_remainder_z
      - .offset:         376
        .size:           8
        .value_kind:     hidden_global_offset_x
      - .offset:         384
        .size:           8
        .value_kind:     hidden_global_offset_y
      - .offset:         392
        .size:           8
        .value_kind:     hidden_global_offset_z
      - .offset:         400
        .size:           2
        .value_kind:     hidden_grid_dims
      - .offset:         456
        .size:           4
        .value_kind:     hidden_dynamic_lds_size
    .group_segment_fixed_size: 0
    .kernarg_segment_align: 8
    .kernarg_segment_size: 592
    .language:       OpenCL C
    .language_version:
      - 2
      - 0
    .max_flat_workgroup_size: 512
    .name:           _Z3fwd4Args
    .private_segment_fixed_size: 0
    .sgpr_count:     108
    .sgpr_spill_count: 18
    .symbol:         _Z3fwd4Args.kd
    .uniform_work_group_size: 1
    .uses_dynamic_stack: false
    .vgpr_count:     256
    .vgpr_spill_count: 0
    .wavefront_size: 64
